# bundle2: + conv staging loads pipelined, gla_out norm-gain hoisted and gate bias via LDS
# speedup vs baseline: 1.0109x; 1.0003x over previous
.LBB0_570:
	s_or_b64 exec, exec, s[70:71]
	v_readlane_b32 s71, v254, 12
	s_waitcnt lgkmcnt(0)
	s_barrier
	v_mbcnt_lo_u32_b32 v8, -1, 0
	v_mbcnt_hi_u32_b32 v8, -1, v8
	v_readlane_b32 s8, v254, 60
	v_and_b32_e32 v68, 63, v8
	s_lshl_b32 s49, s71, 6
	v_or_b32_e32 v2, s8, v68
	v_mov_b64_e32 v[0:1], s[64:65]
	v_add_u32_e32 v67, s49, v8
	v_writelane_b32 v255, s45, 46
	v_mad_u64_u32 v[2:3], s[6:7], v2, s1, v[0:1]
	v_readlane_b32 s6, v255, 45
	s_lshl_b32 s30, s71, 3
	v_ashrrev_i32_e32 v72, 4, v67
	v_readlane_b32 s9, v254, 61
	v_add_u32_e32 v3, s6, v3
	s_ashr_i32 s31, s30, 31
	v_ashrrev_i32_e32 v73, 31, v72
	v_lshl_add_u64 v[4:5], s[30:31], 1, v[2:3]
	v_lshl_add_u64 v[2:3], s[8:9], 0, v[72:73]
	v_mad_u64_u32 v[6:7], s[6:7], v2, s1, v[0:1]
	v_add_u32_e32 v71, 0x200, v67
	v_mov_b32_e32 v2, v7
	v_ashrrev_i32_e32 v74, 4, v71
	v_mad_u64_u32 v[2:3], s[6:7], v3, s1, v[2:3]
	v_ashrrev_i32_e32 v75, 31, v74
	v_mov_b32_e32 v7, v2
	v_lshl_add_u64 v[2:3], s[8:9], 0, v[74:75]
	v_mad_u64_u32 v[0:1], s[6:7], v2, s1, v[0:1]
	v_mov_b32_e32 v2, v1
	v_lshlrev_b32_e32 v69, 3, v67
	v_mad_u64_u32 v[2:3], s[6:7], v3, s1, v[2:3]
	v_and_b32_e32 v70, 0x78, v69
	v_readlane_b32 s6, v254, 38
	v_and_b32_e32 v76, 0xffffff80, v69
	v_lshlrev_b32_e32 v64, 1, v70
	v_mov_b32_e32 v1, v2
	v_readlane_b32 s7, v254, 39
	v_add_u32_e32 v78, 0x1000, v76
	v_bfe_u32 v10, v8, 4, 2
	s_and_b32 s22, s71, 3
	v_lshl_add_u64 v[16:17], v[0:1], 0, v[64:65]
	v_lshl_add_u64 v[0:1], s[6:7], 0, v[64:65]
	v_ashrrev_i32_e32 v77, 31, v76
	v_ashrrev_i32_e32 v79, 31, v78
	v_and_b32_e32 v9, 15, v8
	v_lshl_add_u64 v[12:13], v[6:7], 0, v[64:65]
	v_lshl_add_u64 v[20:21], v[76:77], 1, v[0:1]
	v_lshl_add_u64 v[24:25], v[78:79], 1, v[0:1]
	s_lshl_b32 s8, s22, 4
	v_lshlrev_b32_e32 v1, 2, v10
	v_bfe_u32 v6, v8, 2, 2
	s_lshl_b32 s66, s45, 7
	s_and_b32 s23, s71, -4
	v_or_b32_e32 v0, s8, v9
	v_sub_u32_e32 v2, v9, v1
	v_lshl_or_b32 v7, v10, 3, v6
	v_or_b32_e32 v6, v1, v6
	v_or_b32_e32 v1, s8, v1
	v_readlane_b32 s8, v254, 42
	v_lshlrev_b32_e32 v28, 4, v9
	v_mov_b32_e32 v29, v65
	v_readlane_b32 s9, v254, 43
	s_cmp_eq_u32 s22, 0
	v_and_b32_e32 v38, 48, v8
	v_lshl_add_u64 v[80:81], s[8:9], 0, v[28:29]
	s_cselect_b64 s[8:9], -1, 0
	s_cmp_lg_u32 s22, 0
	s_cselect_b64 s[34:35], -1, 0
	s_cmp_eq_u32 s22, 1
	s_cselect_b64 s[18:19], -1, 0
	s_cmp_gt_u32 s22, 1
	s_cselect_b64 s[36:37], -1, 0
	s_cmp_eq_u32 s22, 2
	v_lshlrev_b32_e32 v66, 3, v68
	s_cselect_b64 s[20:21], -1, 0
	s_cmp_eq_u32 s22, 3
	v_lshlrev_b32_e32 v8, 4, v8
	s_movk_i32 s62, 0x120
	v_and_b32_e32 v3, 24, v66
	s_cselect_b64 s[38:39], -1, 0
	s_or_b32 s22, s23, 1
	s_or_b32 s24, s23, 2
	s_or_b32 s25, s71, 3
	s_movk_i32 s63, 0x110
	v_and_b32_e32 v40, 0xf0, v8
	v_mul_lo_u32 v8, v72, s62
	v_readlane_b32 s28, v254, 36
	v_cmp_gt_i32_e64 s[10:11], 0, v2
	v_cmp_gt_i32_e64 s[12:13], 1, v2
	v_cmp_gt_i32_e64 s[14:15], 2, v2
	v_cmp_gt_i32_e64 s[16:17], 3, v2
	v_lshl_or_b32 v96, s23, 5, v3
	v_lshl_or_b32 v97, s22, 5, v3
	v_lshl_or_b32 v98, s24, 5, v3
	v_lshl_or_b32 v99, s25, 5, v3
	v_mul_lo_u32 v2, v72, s63
	v_mul_lo_u32 v3, v74, s63
	v_add_u32_e32 v41, 0, v8
	v_mul_lo_u32 v8, v74, s62
	s_lshl_b32 vcc_lo, s71, 4
	v_readlane_b32 s29, v254, 37
	v_mad_u32_u24 v105, v7, s62, 0
	v_mad_u32_u24 v107, v6, s62, 0
	v_mad_u32_u24 v108, v1, s63, 0
	v_readlane_b32 s62, v254, 16
	v_lshl_add_u64 v[82:83], s[28:29], 0, v[64:65]
	v_readlane_b32 s63, v254, 17
	s_load_dwordx2 s[28:29], s[62:63], 0x48
	s_waitcnt lgkmcnt(0)
	s_add_u32 s56, s28, s56
	v_readlane_b32 s26, v255, 4
	s_movk_i32 s45, 0xa0
	s_addc_u32 s57, s29, s57
	s_load_dwordx2 s[28:29], s[62:63], 0x50
	s_waitcnt lgkmcnt(0)
	v_cmp_eq_u32_e64 s[6:7], 0, v9
	v_add_u32_e32 v39, s26, v68
	v_mul_u32_u24_e32 v29, 0xa0, v9
	v_lshl_or_b32 v30, s23, 4, v9
	v_lshl_add_u32 v100, v1, 2, s26
	v_lshl_or_b32 v32, s22, 4, v9
	v_lshl_or_b32 v34, s24, 4, v9
	v_lshl_or_b32 v36, s25, 4, v9
	v_add_u32_e32 v42, 0, v8
	v_cmp_eq_u32_e64 s[26:27], 3, v10
	v_mad_u32_u24 v45, v0, s45, 0
	v_add_u32_e32 v46, 0, v2
	v_add_u32_e32 v47, 0, v3
	global_load_dwordx4 v[0:3], v[4:5], off offset:512
	global_load_dwordx4 v[8:11], v[4:5], off offset:3072
	s_nop 0
	global_load_dwordx4 v[4:7], v[4:5], off
	s_nop 0
	global_load_dwordx4 v[12:15], v[12:13], off offset:1024
	s_nop 0
	global_load_dwordx4 v[16:19], v[16:17], off offset:1024
	s_nop 0
	global_load_dwordx4 v[20:23], v[20:21], off
	s_nop 0
	global_load_dwordx4 v[24:27], v[24:25], off
	s_lshl_b64 s[62:63], s[66:67], 2
	s_add_u32 s28, s28, s62
	v_ashrrev_i32_e32 v31, 31, v30
	v_ashrrev_i32_e32 v33, 31, v32
	v_ashrrev_i32_e32 v35, 31, v34
	v_ashrrev_i32_e32 v37, 31, v36
	s_addc_u32 s29, s29, s63
	v_lshl_add_u64 v[84:85], v[30:31], 2, s[28:29]
	v_lshl_add_u64 v[86:87], v[32:33], 2, s[28:29]
	v_lshl_add_u64 v[88:89], v[34:35], 2, s[28:29]
	v_lshl_add_u64 v[90:91], v[36:37], 2, s[28:29]
	s_lshl_b64 s[28:29], s[30:31], 2
	v_mad_u32_u24 v43, v68, s45, 0
	v_add_u32_e32 v44, 0, v38
	s_add_u32 s56, s56, s28
	s_mov_b32 s70, s59
	s_mov_b32 s59, 0
	v_lshlrev_b32_e32 v101, 1, v30
	v_lshlrev_b32_e32 v102, 1, v32
	v_lshlrev_b32_e32 v103, 1, v34
	v_lshlrev_b32_e32 v104, 1, v36
	v_cmp_gt_u32_e64 s[22:23], 16, v68
	v_cmp_lt_u32_e64 s[24:25], 31, v68
	v_add_u32_e32 v106, 0xe100, v105
	v_add_u32_e32 v109, 0x110, v108
	v_add_u32_e32 v110, 0x220, v108
	v_add_u32_e32 v111, 0x330, v108
	s_addc_u32 s57, s57, s29
	v_add_u32_e32 v112, v41, v40
	v_add_u32_e32 v113, v42, v40
	v_add_u32_e32 v114, vcc_lo, v43
	v_add_u32_e32 v115, v45, v38
	v_add_u32_e32 v116, v46, v28
	v_add_u32_e32 v117, v47, v28
	v_add_u32_e32 v118, v44, v29
	v_add_u32_e32 v119, s49, v39
	global_load_dword v204, v[84:85], off
	global_load_dword v205, v[86:87], off
	global_load_dword v206, v[88:89], off
	global_load_dword v207, v[90:91], off
	v_mbcnt_lo_u32_b32 v208, -1, 0
	v_mbcnt_hi_u32_b32 v208, -1, v208
	v_lshrrev_b32_e32 v209, 3, v208
	v_lshlrev_b32_e32 v209, 8, v209
	v_and_b32_e32 v210, 7, v208
	v_lshl_or_b32 v209, v210, 2, v209
	s_lshl_b32 s28, s71, 5
	v_mov_b32_e32 v201, s28
	v_add_u32_e32 v201, 0x24100, v201
	v_cmp_gt_u32_e32 vcc, 32, v208
	s_and_saveexec_b64 s[28:29], vcc
	global_load_dword v210, v209, s[56:57]
	v_add_u32_e32 v209, v201, v209
	s_waitcnt vmcnt(0)
	ds_write_b32 v209, v210
	s_or_b64 exec, exec, s[28:29]
	s_waitcnt lgkmcnt(0)
	s_branch .LBB0_572
.LBB0_571:
	s_or_b64 exec, exec, s[28:29]
	s_waitcnt lgkmcnt(0)
	s_barrier
	ds_read_b128 v[52:55], v100
	ds_read_b128 v[56:59], v100 offset:256
	s_lshl_b32 s28, s49, 7
	s_lshl_b32 s66, s28, 1
	s_add_i32 s59, s59, 1
	s_cmp_lg_u32 s59, 16
	s_waitcnt lgkmcnt(0)
	v_add_f32_e32 v52, v52, v56
	v_fmamk_f32 v52, v52, 0x3c000000, v229
	v_rsq_f32_e32 v52, v52
	s_nop 0
	v_mul_f32_e32 v56, v36, v52
	v_mov_b32_e32 v36, v204
	s_waitcnt vmcnt(0)
	v_mul_f32_e32 v56, v36, v56
	v_bfe_u32 v60, v56, 16, 1
	v_add3_u32 v56, v56, v60, s60
	v_add_u32_e32 v60, v108, v101
	ds_write_b16_d16_hi v60, v56 offset:57600
	v_mul_f32_e32 v56, v40, v52
	v_mov_b32_e32 v40, v205
	v_mul_f32_e32 v56, v40, v56
	v_bfe_u32 v60, v56, 16, 1
	v_add3_u32 v56, v56, v60, s60
	v_add_u32_e32 v60, v108, v102
	ds_write_b16_d16_hi v60, v56 offset:57600
	v_mul_f32_e32 v56, v44, v52
	v_mov_b32_e32 v44, v206
	v_mul_f32_e32 v52, v48, v52
	v_mov_b32_e32 v48, v207
	v_mul_f32_e32 v56, v44, v56
	v_bfe_u32 v60, v56, 16, 1
	v_add3_u32 v56, v56, v60, s60
	v_add_u32_e32 v60, v108, v103
	v_mul_f32_e32 v52, v52, v48
	ds_write_b16_d16_hi v60, v56 offset:57600
	v_bfe_u32 v56, v52, 16, 1
	v_add3_u32 v52, v52, v56, s60
	v_add_u32_e32 v56, v108, v104
	ds_write_b16_d16_hi v56, v52 offset:57600
	v_add_f32_e32 v52, v53, v57
	v_fmamk_f32 v52, v52, 0x3c000000, v229
	v_rsq_f32_e32 v52, v52
	s_nop 0
	v_mul_f32_e32 v37, v37, v52
	v_mul_f32_e32 v37, v36, v37
	v_bfe_u32 v53, v37, 16, 1
	v_add3_u32 v37, v37, v53, s60
	v_add_u32_e32 v53, v109, v101
	ds_write_b16_d16_hi v53, v37 offset:57600
	v_mul_f32_e32 v37, v41, v52
	v_mul_f32_e32 v37, v40, v37
	v_bfe_u32 v41, v37, 16, 1
	v_add3_u32 v37, v37, v41, s60
	v_add_u32_e32 v41, v109, v102
	ds_write_b16_d16_hi v41, v37 offset:57600
	v_mul_f32_e32 v37, v45, v52
	v_mul_f32_e32 v37, v44, v37
	v_bfe_u32 v41, v37, 16, 1
	v_add3_u32 v37, v37, v41, s60
	v_add_u32_e32 v41, v109, v103
	ds_write_b16_d16_hi v41, v37 offset:57600
	v_mul_f32_e32 v37, v49, v52
	v_mul_f32_e32 v37, v48, v37
	v_bfe_u32 v41, v37, 16, 1
	v_add3_u32 v37, v37, v41, s60
	v_add_u32_e32 v41, v109, v104
	ds_write_b16_d16_hi v41, v37 offset:57600
	v_add_f32_e32 v37, v54, v58
	v_fmamk_f32 v37, v37, 0x3c000000, v229
	v_rsq_f32_e32 v37, v37
	v_and_b32_e32 v45, 0xffff0000, v32
	v_mul_f32_e32 v38, v38, v37
	v_mul_f32_e32 v38, v36, v38
	v_bfe_u32 v41, v38, 16, 1
	v_add3_u32 v38, v38, v41, s60
	v_add_u32_e32 v41, v110, v101
	ds_write_b16_d16_hi v41, v38 offset:57600
	v_mul_f32_e32 v38, v42, v37
	v_mul_f32_e32 v38, v40, v38
	v_bfe_u32 v41, v38, 16, 1
	v_add3_u32 v38, v38, v41, s60
	v_add_u32_e32 v41, v110, v102
	ds_write_b16_d16_hi v41, v38 offset:57600
	v_mul_f32_e32 v38, v46, v37
	v_mul_f32_e32 v38, v44, v38
	v_bfe_u32 v41, v38, 16, 1
	v_mul_f32_e32 v37, v50, v37
	v_add3_u32 v38, v38, v41, s60
	v_add_u32_e32 v41, v110, v103
	v_mul_f32_e32 v37, v48, v37
	ds_write_b16_d16_hi v41, v38 offset:57600
	v_bfe_u32 v38, v37, 16, 1
	v_add3_u32 v37, v37, v38, s60
	v_add_u32_e32 v38, v110, v104
	ds_write_b16_d16_hi v38, v37 offset:57600
	v_add_f32_e32 v37, v55, v59
	v_fmamk_f32 v37, v37, 0x3c000000, v229
	v_rsq_f32_e32 v37, v37
	s_nop 0
	v_mul_f32_e32 v38, v39, v37
	v_mul_f32_e32 v36, v36, v38
	v_bfe_u32 v38, v36, 16, 1
	v_add3_u32 v36, v36, v38, s60
	v_add_u32_e32 v38, v111, v101
	ds_write_b16_d16_hi v38, v36 offset:57600
	v_mul_f32_e32 v36, v43, v37
	v_mul_f32_e32 v36, v40, v36
	v_bfe_u32 v38, v36, 16, 1
	v_add3_u32 v36, v36, v38, s60
	v_add_u32_e32 v38, v111, v102
	ds_write_b16_d16_hi v38, v36 offset:57600
	v_mul_f32_e32 v36, v47, v37
	v_mul_f32_e32 v36, v44, v36
	v_lshlrev_b32_e32 v44, 16, v32
	v_mul_f32_e32 v32, 0xbfb8aa3b, v44
	v_exp_f32_e32 v32, v32
	v_bfe_u32 v38, v36, 16, 1
	v_add3_u32 v36, v36, v38, s60
	v_add_u32_e32 v38, v111, v103
	v_add_f32_e32 v32, 1.0, v32
	v_rcp_f32_e32 v46, v32
	v_mul_f32_e32 v32, 0xbfb8aa3b, v45
	ds_write_b16_d16_hi v38, v36 offset:57600
	v_mul_f32_e32 v36, v51, v37
	v_exp_f32_e32 v32, v32
	v_mul_f32_e32 v36, v48, v36
	v_bfe_u32 v37, v36, 16, 1
	v_add3_u32 v36, v36, v37, s60
	v_add_u32_e32 v37, v111, v104
	ds_write_b16_d16_hi v37, v36 offset:57600
	s_waitcnt lgkmcnt(0)
	s_barrier
	ds_read_b128 v[38:41], v116 offset:57600
	v_add_f32_e32 v32, 1.0, v32
	v_rcp_f32_e32 v47, v32
	v_lshlrev_b32_e32 v32, 16, v33
	v_and_b32_e32 v33, 0xffff0000, v33
	s_waitcnt lgkmcnt(0)
	v_lshlrev_b32_e32 v42, 16, v38
	v_and_b32_e32 v43, 0xffff0000, v38
	v_pk_mul_f32 v[44:45], v[46:47], v[44:45]
	v_lshlrev_b32_e32 v38, 16, v39
	v_pk_mul_f32 v[42:43], v[44:45], v[42:43]
	v_mul_f32_e32 v44, 0xbfb8aa3b, v32
	v_mul_f32_e32 v45, 0xbfb8aa3b, v33
	v_exp_f32_e32 v44, v44
	v_exp_f32_e32 v45, v45
	v_and_b32_e32 v39, 0xffff0000, v39
	v_lshl_add_u64 v[36:37], v[80:81], 0, s[66:67]
	v_add_f32_e32 v44, 1.0, v44
	v_add_f32_e32 v45, 1.0, v45
	v_rcp_f32_e32 v44, v44
	v_rcp_f32_e32 v45, v45
	s_nop 0
	v_pk_mul_f32 v[32:33], v[44:45], v[32:33]
	v_lshlrev_b32_e32 v44, 16, v34
	v_and_b32_e32 v45, 0xffff0000, v34
	v_mul_f32_e32 v34, 0xbfb8aa3b, v44
	v_exp_f32_e32 v34, v34
	v_pk_mul_f32 v[38:39], v[32:33], v[38:39]
	v_lshlrev_b32_e32 v32, 16, v40
	v_and_b32_e32 v33, 0xffff0000, v40
	v_add_f32_e32 v34, 1.0, v34
	v_rcp_f32_e32 v46, v34
	v_mul_f32_e32 v34, 0xbfb8aa3b, v45
	v_exp_f32_e32 v34, v34
	s_nop 0
	v_add_f32_e32 v34, 1.0, v34
	v_rcp_f32_e32 v47, v34
	v_lshlrev_b32_e32 v34, 16, v35
	v_and_b32_e32 v35, 0xffff0000, v35
	v_mul_f32_e32 v40, 0xbfb8aa3b, v34
	v_pk_mul_f32 v[44:45], v[46:47], v[44:45]
	v_exp_f32_e32 v40, v40
	v_pk_mul_f32 v[44:45], v[44:45], v[32:33]
	v_lshlrev_b32_e32 v32, 16, v41
	v_and_b32_e32 v33, 0xffff0000, v41
	v_mul_f32_e32 v41, 0xbfb8aa3b, v35
	v_exp_f32_e32 v41, v41
	v_add_f32_e32 v40, 1.0, v40
	v_rcp_f32_e32 v40, v40
	v_add_f32_e32 v41, 1.0, v41
	v_rcp_f32_e32 v41, v41
	s_nop 0
	v_pk_mul_f32 v[34:35], v[40:41], v[34:35]
	s_nop 0
	v_pk_mul_f32 v[40:41], v[34:35], v[32:33]
	v_cvt_pk_bf16_f32 v32, v42, v43
	v_cvt_pk_bf16_f32 v35, v40, v41
	v_lshlrev_b32_e32 v40, 16, v28
	v_and_b32_e32 v41, 0xffff0000, v28
	v_mul_f32_e32 v28, 0xbfb8aa3b, v40
	v_exp_f32_e32 v28, v28
	v_cvt_pk_bf16_f32 v33, v38, v39
	v_lshlrev_b64 v[38:39], 11, v[94:95]
	v_cvt_pk_bf16_f32 v34, v44, v45
	v_add_f32_e32 v28, 1.0, v28
	v_rcp_f32_e32 v42, v28
	v_mul_f32_e32 v28, 0xbfb8aa3b, v41
	v_exp_f32_e32 v28, v28
	v_lshl_add_u64 v[38:39], v[36:37], 0, v[38:39]
	global_store_dwordx4 v[38:39], v[32:35], off
	ds_read_b128 v[32:35], v117 offset:57600
	v_add_f32_e32 v28, 1.0, v28
	v_rcp_f32_e32 v43, v28
	v_lshlrev_b32_e32 v28, 16, v29
	v_and_b32_e32 v29, 0xffff0000, v29
	s_waitcnt lgkmcnt(0)
	v_lshlrev_b32_e32 v38, 16, v32
	v_and_b32_e32 v39, 0xffff0000, v32
	v_pk_mul_f32 v[40:41], v[42:43], v[40:41]
	v_lshlrev_b32_e32 v32, 16, v33
	v_pk_mul_f32 v[38:39], v[40:41], v[38:39]
	v_mul_f32_e32 v40, 0xbfb8aa3b, v28
	v_mul_f32_e32 v41, 0xbfb8aa3b, v29
	v_exp_f32_e32 v40, v40
	v_exp_f32_e32 v41, v41
	v_and_b32_e32 v33, 0xffff0000, v33
	v_add_f32_e32 v40, 1.0, v40
	v_add_f32_e32 v41, 1.0, v41
	v_rcp_f32_e32 v40, v40
	v_rcp_f32_e32 v41, v41
	s_nop 0
	v_pk_mul_f32 v[28:29], v[40:41], v[28:29]
	v_lshlrev_b32_e32 v40, 16, v30
	v_and_b32_e32 v41, 0xffff0000, v30
	v_mul_f32_e32 v30, 0xbfb8aa3b, v40
	v_exp_f32_e32 v30, v30
	v_pk_mul_f32 v[32:33], v[28:29], v[32:33]
	v_lshlrev_b32_e32 v28, 16, v34
	v_and_b32_e32 v29, 0xffff0000, v34
	v_add_f32_e32 v30, 1.0, v30
	v_rcp_f32_e32 v42, v30
	v_mul_f32_e32 v30, 0xbfb8aa3b, v41
	v_exp_f32_e32 v30, v30
	s_nop 0
	v_add_f32_e32 v30, 1.0, v30
	v_rcp_f32_e32 v43, v30
	v_lshlrev_b32_e32 v30, 16, v31
	v_and_b32_e32 v31, 0xffff0000, v31
	v_mul_f32_e32 v34, 0xbfb8aa3b, v30
	v_pk_mul_f32 v[40:41], v[42:43], v[40:41]
	v_exp_f32_e32 v34, v34
	v_pk_mul_f32 v[40:41], v[40:41], v[28:29]
	v_lshlrev_b32_e32 v28, 16, v35
	v_and_b32_e32 v29, 0xffff0000, v35
	v_mul_f32_e32 v35, 0xbfb8aa3b, v31
	v_exp_f32_e32 v35, v35
	v_add_f32_e32 v34, 1.0, v34
	v_rcp_f32_e32 v34, v34
	v_add_f32_e32 v35, 1.0, v35
	v_rcp_f32_e32 v35, v35
	s_nop 0
	v_pk_mul_f32 v[30:31], v[34:35], v[30:31]
	s_nop 0
	v_pk_mul_f32 v[34:35], v[30:31], v[28:29]
	v_cvt_pk_bf16_f32 v29, v32, v33
	v_lshlrev_b64 v[32:33], 11, v[92:93]
	v_cvt_pk_bf16_f32 v28, v38, v39
	v_cvt_pk_bf16_f32 v30, v40, v41
	v_cvt_pk_bf16_f32 v31, v34, v35
	v_lshl_add_u64 v[32:33], v[36:37], 0, v[32:33]
	global_store_dwordx4 v[32:33], v[28:31], off
	s_cbranch_scc0 .LBB0_596
.LBB0_572:
	s_lshr_b32 s28, s59, 2
	s_add_i32 s28, s28, s3
	s_lshl_b32 s28, s28, 6
	s_or_b32 s28, s82, s28
	s_mov_b32 s29, s83
	v_lshl_add_u64 v[94:95], s[28:29], 0, v[72:73]
	v_mov_b64_e32 v[28:29], s[64:65]
	v_lshl_add_u64 v[92:93], s[28:29], 0, v[74:75]
	s_and_b32 s49, s59, 3
	v_mad_u64_u32 v[30:31], s[62:63], v94, s1, v[28:29]
	v_mad_u64_u32 v[28:29], s[28:29], v92, s1, v[28:29]
	v_mad_i32_i24 v31, v95, s1, v31
	s_lshl_b32 s66, s49, 8
	v_mad_i32_i24 v29, v93, s1, v29
	v_lshl_add_u64 v[30:31], v[30:31], 0, s[66:67]
	v_lshlrev_b32_e32 v64, 1, v70
	v_lshl_add_u64 v[28:29], v[28:29], 0, s[66:67]
	v_lshl_add_u64 v[30:31], v[30:31], 0, v[64:65]
	v_lshl_add_u64 v[28:29], v[28:29], 0, v[64:65]
	global_load_dwordx4 v[32:35], v[30:31], off offset:2048
	v_mov_b32_e32 v40, s66
	global_load_dwordx4 v[28:31], v[28:29], off offset:2048
	s_barrier
	s_waitcnt vmcnt(2)
	ds_write_b128 v112, v[12:15] offset:39168
	ds_write_b128 v113, v[16:19] offset:39168
	ds_write_b128 v112, v[20:23] offset:57600
	ds_write_b128 v113, v[24:27] offset:57600
	v_add_u32_e32 v40, v201, v40
	ds_read_b128 v[36:39], v40 offset:16
	ds_read_b128 v[40:43], v40
	v_lshlrev_b32_e32 v44, 16, v8
	v_and_b32_e32 v45, 0xffff0000, v8
	v_lshlrev_b32_e32 v47, 16, v9
	v_and_b32_e32 v46, 0xffff0000, v9
	v_lshlrev_b32_e32 v51, 16, v10
	v_and_b32_e32 v50, 0xffff0000, v10
	v_lshlrev_b32_e32 v52, 16, v4
	v_and_b32_e32 v53, 0xffff0000, v4
	s_mov_b32 s66, 0x3e000000
	v_pk_mul_f32 v[52:53], v[52:53], s[66:67] op_sel_hi:[1,0]
	v_lshlrev_b32_e32 v49, 16, v11
	v_and_b32_e32 v48, 0xffff0000, v11
	s_cmp_eq_u32 s59, 15
	s_waitcnt lgkmcnt(1)
	v_add_f32_e32 v36, v36, v51
	s_waitcnt lgkmcnt(0)
	v_add_f32_e32 v40, v40, v44
	v_min_f32_e32 v44, 0, v40
	v_mul_f32_e64 v40, |v40|, s0
	v_exp_f32_e32 v40, v40
	v_add_f32_e32 v41, v41, v45
	v_min_f32_e32 v45, 0, v41
	v_mul_f32_e64 v41, |v41|, s0
	v_exp_f32_e32 v41, v41
	v_add_f32_e32 v40, 1.0, v40
	v_log_f32_e32 v40, v40
	v_add_f32_e32 v42, v42, v47
	v_add_f32_e32 v41, 1.0, v41
	v_min_f32_e32 v47, 0, v42
	v_mul_f32_e64 v42, |v42|, s0
	v_log_f32_e32 v41, v41
	v_exp_f32_e32 v42, v42
	v_add_f32_e32 v43, v43, v46
	v_min_f32_e32 v46, 0, v43
	v_mul_f32_e64 v43, |v43|, s0
	v_fmac_f32_e32 v44, 0xbf317218, v40
	v_exp_f32_e32 v43, v43
	v_mul_f32_e32 v40, 0x3d800000, v44
	v_fmac_f32_e32 v45, 0xbf317218, v41
	v_add_f32_e32 v42, 1.0, v42
	v_mov_b32_dpp v40, v40 row_shr:1 row_mask:0xf bank_mask:0xf bound_ctrl:1
	v_fmac_f32_e32 v40, 0x3d800000, v44
	v_mul_f32_e32 v41, 0x3d800000, v45
	v_log_f32_e32 v42, v42
	v_add_f32_dpp v40, v40, v40 row_shr:2 row_mask:0xf bank_mask:0xf bound_ctrl:1
	v_mov_b32_dpp v41, v41 row_shr:1 row_mask:0xf bank_mask:0xf bound_ctrl:1
	v_add_f32_e32 v43, 1.0, v43
	v_add_f32_dpp v40, v40, v40 row_shr:4 row_mask:0xf bank_mask:0xf bound_ctrl:1
	v_fmac_f32_e32 v41, 0x3d800000, v45
	v_log_f32_e32 v43, v43
	v_add_f32_dpp v40, v40, v40 row_shr:8 row_mask:0xf bank_mask:0xf bound_ctrl:1
	v_add_f32_dpp v41, v41, v41 row_shr:2 row_mask:0xf bank_mask:0xf bound_ctrl:1
	v_readlane_b32 s28, v40, 15
	v_fmac_f32_e32 v47, 0xbf317218, v42
	v_add_f32_dpp v41, v41, v41 row_shr:4 row_mask:0xf bank_mask:0xf bound_ctrl:1
	v_mov_b32_e32 v44, s28
	v_mul_f32_e32 v42, 0x3d800000, v47
	v_add_f32_dpp v41, v41, v41 row_shr:8 row_mask:0xf bank_mask:0xf bound_ctrl:1
	v_min_f32_e32 v51, 0, v36
	v_mul_f32_e64 v36, |v36|, s0
	v_readlane_b32 s29, v40, 31
	v_cndmask_b32_e64 v44, v44, 0, s[22:23]
	v_readlane_b32 s28, v41, 15
	v_mov_b32_dpp v42, v42 row_shr:1 row_mask:0xf bank_mask:0xf bound_ctrl:1
	v_fmac_f32_e32 v46, 0xbf317218, v43
	v_exp_f32_e32 v36, v36
	v_add_f32_e32 v37, v37, v50
	v_readlane_b32 s62, v40, 47
	v_add_f32_e32 v40, v44, v40
	v_mov_b32_e32 v44, s29
	v_mov_b32_e32 v45, s28
	v_fmac_f32_e32 v42, 0x3d800000, v47
	v_mul_f32_e32 v43, 0x3d800000, v46
	v_min_f32_e32 v50, 0, v37
	v_mul_f32_e64 v37, |v37|, s0
	v_cndmask_b32_e64 v44, 0, v44, s[24:25]
	v_readlane_b32 s29, v41, 31
	v_cndmask_b32_e64 v45, v45, 0, s[22:23]
	v_add_f32_dpp v42, v42, v42 row_shr:2 row_mask:0xf bank_mask:0xf bound_ctrl:1
	v_mov_b32_dpp v43, v43 row_shr:1 row_mask:0xf bank_mask:0xf bound_ctrl:1
	v_exp_f32_e32 v37, v37
	v_add_f32_e32 v40, v44, v40
	v_mov_b32_e32 v44, s62
	v_readlane_b32 s62, v41, 47
	v_add_f32_e32 v41, v41, v45
	v_mov_b32_e32 v45, s29
	v_add_f32_dpp v42, v42, v42 row_shr:4 row_mask:0xf bank_mask:0xf bound_ctrl:1
	v_fmac_f32_e32 v43, 0x3d800000, v46
	v_cndmask_b32_e64 v45, 0, v45, s[24:25]
	v_add_f32_dpp v42, v42, v42 row_shr:8 row_mask:0xf bank_mask:0xf bound_ctrl:1
	v_add_f32_dpp v43, v43, v43 row_shr:2 row_mask:0xf bank_mask:0xf bound_ctrl:1
	v_add_f32_e32 v36, 1.0, v36
	v_add_f32_e32 v41, v41, v45
	v_mov_b32_e32 v45, s62
	v_readlane_b32 s28, v42, 15
	v_add_f32_dpp v43, v43, v43 row_shr:4 row_mask:0xf bank_mask:0xf bound_ctrl:1
	v_log_f32_e32 v36, v36
	v_cndmask_b32_e64 v44, 0, v44, s[26:27]
	v_cndmask_b32_e64 v45, 0, v45, s[26:27]
	v_mov_b32_e32 v47, s28
	v_add_f32_dpp v43, v43, v43 row_shr:8 row_mask:0xf bank_mask:0xf bound_ctrl:1
	v_add_f32_e32 v37, 1.0, v37
	v_add_f32_e32 v44, v44, v40
	v_add_f32_e32 v45, v41, v45
	v_readlane_b32 s29, v42, 31
	v_cndmask_b32_e64 v47, v47, 0, s[22:23]
	v_readlane_b32 s28, v43, 15
	v_log_f32_e32 v37, v37
	v_mul_f32_e32 v40, 0x3fb8aa3b, v44
	v_mul_f32_e32 v41, 0x3fb8aa3b, v45
	v_readlane_b32 s62, v42, 47
	v_add_f32_e32 v42, v42, v47
	v_mov_b32_e32 v47, s29
	v_mov_b32_e32 v46, s28
	v_exp_f32_e32 v40, v40
	v_mul_f32_e32 v44, 0xbfb8aa3b, v44
	v_exp_f32_e32 v41, v41
	v_mul_f32_e32 v45, 0xbfb8aa3b, v45
	v_cndmask_b32_e64 v47, 0, v47, s[24:25]
	v_readlane_b32 s29, v43, 31
	v_cndmask_b32_e64 v46, v46, 0, s[22:23]
	v_fmac_f32_e32 v51, 0xbf317218, v36
	v_exp_f32_e32 v44, v44
	v_exp_f32_e32 v45, v45
	v_add_f32_e32 v42, v42, v47
	v_mov_b32_e32 v47, s62
	v_readlane_b32 s62, v43, 47
	v_add_f32_e32 v43, v43, v46
	v_mov_b32_e32 v46, s29
	v_mul_f32_e32 v36, 0x3d800000, v51
	v_cndmask_b32_e64 v46, 0, v46, s[24:25]
	v_fmac_f32_e32 v50, 0xbf317218, v37
	v_mov_b32_dpp v36, v36 row_shr:1 row_mask:0xf bank_mask:0xf bound_ctrl:1
	v_add_f32_e32 v43, v43, v46
	v_mov_b32_e32 v46, s62
	v_fmac_f32_e32 v36, 0x3d800000, v51
	v_mul_f32_e32 v37, 0x3d800000, v50
	v_pk_mul_f32 v[40:41], v[52:53], v[40:41]
	v_lshlrev_b32_e32 v52, 16, v0
	v_and_b32_e32 v53, 0xffff0000, v0
	v_cndmask_b32_e64 v47, 0, v47, s[26:27]
	v_cndmask_b32_e64 v46, 0, v46, s[26:27]
	v_add_f32_dpp v36, v36, v36 row_shr:2 row_mask:0xf bank_mask:0xf bound_ctrl:1
	v_mov_b32_dpp v37, v37 row_shr:1 row_mask:0xf bank_mask:0xf bound_ctrl:1
	v_pk_mul_f32 v[44:45], v[44:45], v[52:53]
	v_add_f32_e32 v47, v42, v47
	v_add_f32_e32 v53, v43, v46
	v_add_f32_dpp v36, v36, v36 row_shr:4 row_mask:0xf bank_mask:0xf bound_ctrl:1
	v_fmac_f32_e32 v37, 0x3d800000, v50
	v_mul_f32_e32 v42, 0x3fb8aa3b, v47
	v_mul_f32_e32 v43, 0x3fb8aa3b, v53
	v_add_f32_dpp v36, v36, v36 row_shr:8 row_mask:0xf bank_mask:0xf bound_ctrl:1
	v_add_f32_dpp v37, v37, v37 row_shr:2 row_mask:0xf bank_mask:0xf bound_ctrl:1
	v_exp_f32_e32 v42, v42
	v_exp_f32_e32 v43, v43
	v_readlane_b32 s28, v36, 15
	v_add_f32_dpp v37, v37, v37 row_shr:4 row_mask:0xf bank_mask:0xf bound_ctrl:1
	v_mul_f32_e32 v47, 0xbfb8aa3b, v47
	v_mov_b32_e32 v51, s28
	v_add_f32_dpp v37, v37, v37 row_shr:8 row_mask:0xf bank_mask:0xf bound_ctrl:1
	v_exp_f32_e32 v52, v47
	v_lshlrev_b32_e32 v46, 16, v5
	v_and_b32_e32 v47, 0xffff0000, v5
	v_readlane_b32 s29, v36, 31
	v_cndmask_b32_e64 v51, v51, 0, s[22:23]
	v_readlane_b32 s28, v37, 15
	v_pk_mul_f32 v[46:47], v[46:47], s[66:67] op_sel_hi:[1,0]
	v_readlane_b32 s62, v36, 47
	v_add_f32_e32 v36, v36, v51
	v_mov_b32_e32 v51, s29
	v_mov_b32_e32 v50, s28
	v_pk_mul_f32 v[42:43], v[46:47], v[42:43]
	v_mul_f32_e32 v46, 0xbfb8aa3b, v53
	v_cndmask_b32_e64 v51, 0, v51, s[24:25]
	v_readlane_b32 s29, v37, 31
	v_cndmask_b32_e64 v50, v50, 0, s[22:23]
	v_exp_f32_e32 v53, v46
	v_add_f32_e32 v36, v36, v51
	v_mov_b32_e32 v51, s62
	v_readlane_b32 s62, v37, 47
	v_add_f32_e32 v37, v37, v50
	v_mov_b32_e32 v50, s29
	v_cndmask_b32_e64 v50, 0, v50, s[24:25]
	v_add_f32_e32 v37, v37, v50
	v_mov_b32_e32 v50, s62
	v_lshlrev_b32_e32 v46, 16, v1
	v_and_b32_e32 v47, 0xffff0000, v1
	v_cndmask_b32_e64 v51, 0, v51, s[26:27]
	v_cndmask_b32_e64 v50, 0, v50, s[26:27]
	v_pk_mul_f32 v[46:47], v[52:53], v[46:47]
	v_add_f32_e32 v51, v36, v51
	v_add_f32_e32 v53, v37, v50
	v_mul_f32_e32 v36, 0x3fb8aa3b, v51
	v_mul_f32_e32 v37, 0x3fb8aa3b, v53
	v_exp_f32_e32 v36, v36
	v_exp_f32_e32 v37, v37
	v_mul_f32_e32 v51, 0xbfb8aa3b, v51
	v_exp_f32_e32 v52, v51
	v_lshlrev_b32_e32 v50, 16, v6
	v_and_b32_e32 v51, 0xffff0000, v6
	v_pk_mul_f32 v[50:51], v[50:51], s[66:67] op_sel_hi:[1,0]
	s_nop 0
	v_pk_mul_f32 v[50:51], v[50:51], v[36:37]
	v_mul_f32_e32 v36, 0xbfb8aa3b, v53
	v_exp_f32_e32 v53, v36
	v_lshlrev_b32_e32 v36, 16, v2
	v_and_b32_e32 v37, 0xffff0000, v2
	v_pk_mul_f32 v[52:53], v[52:53], v[36:37]
	v_add_f32_e32 v36, v38, v49
	v_min_f32_e32 v37, 0, v36
	v_mul_f32_e64 v36, |v36|, s0
	v_exp_f32_e32 v36, v36
	v_and_b32_e32 v49, 0xffff0000, v7
	v_add_f32_e32 v36, 1.0, v36
	v_log_f32_e32 v36, v36
	s_nop 0
	v_fmac_f32_e32 v37, 0xbf317218, v36
	v_mul_f32_e32 v36, 0x3d800000, v37
	s_nop 1
	v_mov_b32_dpp v36, v36 row_shr:1 row_mask:0xf bank_mask:0xf bound_ctrl:1
	v_fmac_f32_e32 v36, 0x3d800000, v37
	s_nop 1
	v_add_f32_dpp v36, v36, v36 row_shr:2 row_mask:0xf bank_mask:0xf bound_ctrl:1
	s_nop 1
	v_add_f32_dpp v36, v36, v36 row_shr:4 row_mask:0xf bank_mask:0xf bound_ctrl:1
	s_nop 1
	v_add_f32_dpp v36, v36, v36 row_shr:8 row_mask:0xf bank_mask:0xf bound_ctrl:1
	s_nop 0
	v_readlane_b32 s28, v36, 15
	v_readlane_b32 s29, v36, 31
	v_readlane_b32 s62, v36, 47
	v_mov_b32_e32 v37, s28
	v_cndmask_b32_e64 v37, v37, 0, s[22:23]
	v_add_f32_e32 v36, v36, v37
	v_mov_b32_e32 v37, s29
	v_cndmask_b32_e64 v37, 0, v37, s[24:25]
	v_add_f32_e32 v36, v36, v37
	v_mov_b32_e32 v37, s62
	v_cndmask_b32_e64 v37, 0, v37, s[26:27]
	v_add_f32_e32 v37, v36, v37
	v_mul_f32_e32 v36, 0x3fb8aa3b, v37
	v_mul_f32_e32 v37, 0xbfb8aa3b, v37
	v_exp_f32_e32 v38, v37
	v_add_f32_e32 v37, v39, v48
	v_min_f32_e32 v39, 0, v37
	v_mul_f32_e64 v37, |v37|, s0
	v_exp_f32_e32 v37, v37
	v_exp_f32_e32 v36, v36
	v_lshlrev_b32_e32 v48, 16, v7
	v_pk_mul_f32 v[48:49], v[48:49], s[66:67] op_sel_hi:[1,0]
	v_add_f32_e32 v37, 1.0, v37
	v_log_f32_e32 v37, v37
	s_nop 0
	v_fmac_f32_e32 v39, 0xbf317218, v37
	v_mul_f32_e32 v37, 0x3d800000, v39
	s_nop 1
	v_mov_b32_dpp v37, v37 row_shr:1 row_mask:0xf bank_mask:0xf bound_ctrl:1
	v_fmac_f32_e32 v37, 0x3d800000, v39
	s_nop 1
	v_add_f32_dpp v37, v37, v37 row_shr:2 row_mask:0xf bank_mask:0xf bound_ctrl:1
	s_nop 1
	v_add_f32_dpp v37, v37, v37 row_shr:4 row_mask:0xf bank_mask:0xf bound_ctrl:1
	s_nop 1
	v_add_f32_dpp v37, v37, v37 row_shr:8 row_mask:0xf bank_mask:0xf bound_ctrl:1
	s_nop 0
	v_readlane_b32 s28, v37, 15
	v_readlane_b32 s29, v37, 31
	v_readlane_b32 s62, v37, 47
	v_mov_b32_e32 v39, s28
	v_cndmask_b32_e64 v39, v39, 0, s[22:23]
	v_add_f32_e32 v37, v37, v39
	v_mov_b32_e32 v39, s29
	v_cndmask_b32_e64 v39, 0, v39, s[24:25]
	v_add_f32_e32 v37, v37, v39
	v_mov_b32_e32 v39, s62
	v_cndmask_b32_e64 v39, 0, v39, s[26:27]
	v_add_f32_e32 v39, v37, v39
	v_mul_f32_e32 v37, 0x3fb8aa3b, v39
	v_exp_f32_e32 v37, v37
	s_nop 0
	v_pk_mul_f32 v[48:49], v[48:49], v[36:37]
	v_mul_f32_e32 v36, 0xbfb8aa3b, v39
	v_exp_f32_e32 v39, v36
	v_lshlrev_b32_e32 v36, 16, v3
	v_and_b32_e32 v37, 0xffff0000, v3
	v_pk_mul_f32 v[54:55], v[38:39], v[36:37]
	v_cvt_pk_bf16_f32 v36, v44, v45
	v_cvt_pk_bf16_f32 v37, v46, v47
	v_cvt_pk_bf16_f32 v38, v52, v53
	v_cvt_pk_bf16_f32 v39, v54, v55
	ds_write_b128 v114, v[36:39] offset:28928
	v_cvt_pk_bf16_f32 v36, v40, v41
	v_cvt_pk_bf16_f32 v37, v42, v43
	v_cvt_pk_bf16_f32 v38, v50, v51
	v_cvt_pk_bf16_f32 v39, v48, v49
	ds_write_b128 v114, v[36:39] offset:18688
	s_cbranch_scc1 .LBB0_574
	s_add_i32 s28, s59, 1
	s_and_b32 s29, s28, 3
	s_lshr_b32 s28, s28, 2
	s_add_i32 s62, s28, s3
	s_lshl_b32 s66, s29, 7
	v_readlane_b32 s28, v254, 35
	s_or_b32 s28, s66, s28
	s_add_i32 s28, s28, s62
	s_lshl_b32 s62, s62, 6
	s_add_u32 s62, s82, s62
	v_or_b32_e32 v0, s62, v68
	v_mov_b64_e32 v[16:17], s[64:65]
	s_addc_u32 s63, s83, 0
	v_mad_u64_u32 v[0:1], vcc, v0, s1, v[16:17]
	v_mov_b32_e32 v2, 0x1200
	v_mad_i32_i24 v1, s63, v2, v1
	v_lshl_add_u64 v[10:11], s[62:63], 0, v[72:73]
	v_lshl_add_u64 v[18:19], s[62:63], 0, v[74:75]
	v_lshl_add_u64 v[0:1], v[0:1], 0, s[66:67]
	v_mad_u64_u32 v[12:13], vcc, v10, s1, v[16:17]
	s_lshl_b32 s66, s29, 8
	v_mad_u64_u32 v[16:17], s[62:63], v18, s1, v[16:17]
	s_ashr_i32 s29, s28, 31
	v_mad_i32_i24 v13, v11, s1, v13
	v_mad_i32_i24 v17, v19, s1, v17
	s_lshl_b64 s[28:29], s[28:29], 14
	v_lshl_add_u64 v[10:11], v[12:13], 0, s[66:67]
	v_lshl_add_u64 v[16:17], v[16:17], 0, s[66:67]
	v_lshl_add_u64 v[24:25], v[82:83], 0, s[28:29]
	v_lshl_add_u64 v[8:9], s[30:31], 1, v[0:1]
	v_lshl_add_u64 v[12:13], v[10:11], 0, v[64:65]
	v_lshl_add_u64 v[16:17], v[16:17], 0, v[64:65]
	v_lshl_add_u64 v[20:21], v[76:77], 1, v[24:25]
	v_lshl_add_u64 v[24:25], v[78:79], 1, v[24:25]
	global_load_dwordx4 v[0:3], v[8:9], off offset:512
	global_load_dwordx4 v[4:7], v[8:9], off
	s_nop 0
	global_load_dwordx4 v[8:11], v[8:9], off offset:3072
	s_nop 0
	global_load_dwordx4 v[12:15], v[12:13], off offset:1024
	s_nop 0
	global_load_dwordx4 v[16:19], v[16:17], off offset:1024
	s_nop 0
	global_load_dwordx4 v[20:23], v[20:21], off
	s_nop 0
	global_load_dwordx4 v[24:27], v[24:25], off

.LBB0_598:
	s_barrier
	s_and_saveexec_b64 s[28:29], s[8:9]
	v_mov_b32_e32 v204, 0
	v_mov_b32_e32 v205, 0
	v_mov_b32_e32 v206, 0
	v_mov_b32_e32 v207, 0
	v_add_u32_e32 v64, s75, v184
	v_cmp_lt_i32_e32 vcc, -1, v64
	s_and_saveexec_b64 s[30:31], vcc
	s_cbranch_execz .Lcv_skipA_0
	v_lshl_add_u64 v[0:1], s[82:83], 0, v[64:65]
	v_mov_b64_e32 v[2:3], s[42:43]
	v_mad_u64_u32 v[2:3], s[34:35], v0, s1, v[2:3]
	v_mad_i32_i24 v3, v1, s1, v3
	v_lshlrev_b32_e32 v64, 1, v66
	v_lshl_add_u64 v[0:1], v[2:3], 0, v[64:65]
	v_add_co_u32_e32 v0, vcc, 0x16800000, v0
	s_nop 1
	v_addc_co_u32_e32 v1, vcc, 0, v1, vcc
	global_load_dwordx4 v[204:207], v[0:1], off offset:3584
.Lcv_skipA_0:
	s_or_b64 exec, exec, s[30:31]
	s_or_b64 exec, exec, s[28:29]
	s_and_saveexec_b64 s[28:29], s[10:11]
	v_mov_b32_e32 v208, 0
	v_mov_b32_e32 v209, 0
	v_mov_b32_e32 v210, 0
	v_mov_b32_e32 v211, 0
	v_add_u32_e32 v64, s75, v185
	v_cmp_lt_i32_e32 vcc, -1, v64
	s_and_saveexec_b64 s[30:31], vcc
	s_cbranch_execz .Lcv_skipA_1
	v_lshl_add_u64 v[0:1], s[82:83], 0, v[64:65]
	v_mov_b64_e32 v[2:3], s[42:43]
	v_mad_u64_u32 v[2:3], s[34:35], v0, s1, v[2:3]
	v_mad_i32_i24 v3, v1, s1, v3
	v_lshlrev_b32_e32 v64, 1, v66
	v_lshl_add_u64 v[0:1], v[2:3], 0, v[64:65]
	v_add_co_u32_e32 v0, vcc, 0x16800000, v0
	s_nop 1
	v_addc_co_u32_e32 v1, vcc, 0, v1, vcc
	global_load_dwordx4 v[208:211], v[0:1], off offset:3584
.Lcv_skipA_1:
	s_or_b64 exec, exec, s[30:31]
	s_or_b64 exec, exec, s[28:29]
	s_and_saveexec_b64 s[28:29], s[12:13]
	v_mov_b32_e32 v212, 0
	v_mov_b32_e32 v213, 0
	v_mov_b32_e32 v214, 0
	v_mov_b32_e32 v215, 0
	v_add_u32_e32 v64, s75, v186
	v_cmp_lt_i32_e32 vcc, -1, v64
	s_and_saveexec_b64 s[30:31], vcc
	s_cbranch_execz .Lcv_skipA_2
	v_lshl_add_u64 v[0:1], s[82:83], 0, v[64:65]
	v_mov_b64_e32 v[2:3], s[42:43]
	v_mad_u64_u32 v[2:3], s[34:35], v0, s1, v[2:3]
	v_mad_i32_i24 v3, v1, s1, v3
	v_lshlrev_b32_e32 v64, 1, v66
	v_lshl_add_u64 v[0:1], v[2:3], 0, v[64:65]
	v_add_co_u32_e32 v0, vcc, 0x16800000, v0
	s_nop 1
	v_addc_co_u32_e32 v1, vcc, 0, v1, vcc
	global_load_dwordx4 v[212:215], v[0:1], off offset:3584
.Lcv_skipA_2:
	s_or_b64 exec, exec, s[30:31]
	s_or_b64 exec, exec, s[28:29]
	s_and_saveexec_b64 s[28:29], s[14:15]
	v_mov_b32_e32 v216, 0
	v_mov_b32_e32 v217, 0
	v_mov_b32_e32 v218, 0
	v_mov_b32_e32 v219, 0
	v_add_u32_e32 v64, s75, v187
	v_cmp_lt_i32_e32 vcc, -1, v64
	s_and_saveexec_b64 s[30:31], vcc
	s_cbranch_execz .Lcv_skipA_3
	v_lshl_add_u64 v[0:1], s[82:83], 0, v[64:65]
	v_mov_b64_e32 v[2:3], s[42:43]
	v_mad_u64_u32 v[2:3], s[34:35], v0, s1, v[2:3]
	v_mad_i32_i24 v3, v1, s1, v3
	v_lshlrev_b32_e32 v64, 1, v66
	v_lshl_add_u64 v[0:1], v[2:3], 0, v[64:65]
	v_add_co_u32_e32 v0, vcc, 0x16800000, v0
	s_nop 1
	v_addc_co_u32_e32 v1, vcc, 0, v1, vcc
	global_load_dwordx4 v[216:219], v[0:1], off offset:3584
.Lcv_skipA_3:
	s_or_b64 exec, exec, s[30:31]
	s_or_b64 exec, exec, s[28:29]
	s_and_saveexec_b64 s[28:29], s[16:17]
	v_mov_b32_e32 v220, 0
	v_mov_b32_e32 v221, 0
	v_mov_b32_e32 v222, 0
	v_mov_b32_e32 v223, 0
	v_add_u32_e32 v64, s75, v188
	v_cmp_lt_i32_e32 vcc, -1, v64
	s_and_saveexec_b64 s[30:31], vcc
	s_cbranch_execz .Lcv_skipA_4
	v_lshl_add_u64 v[0:1], s[82:83], 0, v[64:65]
	v_mov_b64_e32 v[2:3], s[42:43]
	v_mad_u64_u32 v[2:3], s[34:35], v0, s1, v[2:3]
	v_mad_i32_i24 v3, v1, s1, v3
	v_lshlrev_b32_e32 v64, 1, v66
	v_lshl_add_u64 v[0:1], v[2:3], 0, v[64:65]
	v_add_co_u32_e32 v0, vcc, 0x16800000, v0
	s_nop 1
	v_addc_co_u32_e32 v1, vcc, 0, v1, vcc
	global_load_dwordx4 v[220:223], v[0:1], off offset:3584
.Lcv_skipA_4:
	s_or_b64 exec, exec, s[30:31]
	s_or_b64 exec, exec, s[28:29]
	s_and_saveexec_b64 s[28:29], s[18:19]
	v_mov_b32_e32 v224, 0
	v_mov_b32_e32 v225, 0
	v_mov_b32_e32 v226, 0
	v_mov_b32_e32 v227, 0
	v_add_u32_e32 v64, s75, v189
	v_cmp_lt_i32_e32 vcc, -1, v64
	s_and_saveexec_b64 s[30:31], vcc
	s_cbranch_execz .Lcv_skipA_5
	v_lshl_add_u64 v[0:1], s[82:83], 0, v[64:65]
	v_mov_b64_e32 v[2:3], s[42:43]
	v_mad_u64_u32 v[2:3], s[34:35], v0, s1, v[2:3]
	v_mad_i32_i24 v3, v1, s1, v3
	v_lshlrev_b32_e32 v64, 1, v66
	v_lshl_add_u64 v[0:1], v[2:3], 0, v[64:65]
	v_add_co_u32_e32 v0, vcc, 0x16800000, v0
	s_nop 1
	v_addc_co_u32_e32 v1, vcc, 0, v1, vcc
	global_load_dwordx4 v[224:227], v[0:1], off offset:3584
.Lcv_skipA_5:
	s_or_b64 exec, exec, s[30:31]
	s_or_b64 exec, exec, s[28:29]
	s_and_saveexec_b64 s[28:29], s[20:21]
	v_mov_b32_e32 v230, 0
	v_mov_b32_e32 v231, 0
	v_mov_b32_e32 v232, 0
	v_mov_b32_e32 v233, 0
	v_add_u32_e32 v64, s75, v190
	v_cmp_lt_i32_e32 vcc, -1, v64
	s_and_saveexec_b64 s[30:31], vcc
	s_cbranch_execz .Lcv_skipA_6
	v_lshl_add_u64 v[0:1], s[82:83], 0, v[64:65]
	v_mov_b64_e32 v[2:3], s[42:43]
	v_mad_u64_u32 v[2:3], s[34:35], v0, s1, v[2:3]
	v_mad_i32_i24 v3, v1, s1, v3
	v_lshlrev_b32_e32 v64, 1, v66
	v_lshl_add_u64 v[0:1], v[2:3], 0, v[64:65]
	v_add_co_u32_e32 v0, vcc, 0x16800000, v0
	s_nop 1
	v_addc_co_u32_e32 v1, vcc, 0, v1, vcc
	global_load_dwordx4 v[230:233], v[0:1], off offset:3584
.Lcv_skipA_6:
	s_or_b64 exec, exec, s[30:31]
	s_or_b64 exec, exec, s[28:29]
	s_and_saveexec_b64 s[28:29], s[22:23]
	v_mov_b32_e32 v234, 0
	v_mov_b32_e32 v235, 0
	v_mov_b32_e32 v236, 0
	v_mov_b32_e32 v237, 0
	v_add_u32_e32 v64, s75, v67
	v_cmp_lt_i32_e32 vcc, -1, v64
	s_and_saveexec_b64 s[30:31], vcc
	s_cbranch_execz .Lcv_skipA_7
	v_lshl_add_u64 v[0:1], s[82:83], 0, v[64:65]
	v_mov_b64_e32 v[2:3], s[42:43]
	v_mad_u64_u32 v[2:3], s[34:35], v0, s1, v[2:3]
	v_mad_i32_i24 v3, v1, s1, v3
	v_lshlrev_b32_e32 v64, 1, v66
	v_lshl_add_u64 v[0:1], v[2:3], 0, v[64:65]
	v_add_co_u32_e32 v0, vcc, 0x16800000, v0
	s_nop 1
	v_addc_co_u32_e32 v1, vcc, 0, v1, vcc
	global_load_dwordx4 v[234:237], v[0:1], off offset:3584
.Lcv_skipA_7:
	s_or_b64 exec, exec, s[30:31]
	s_or_b64 exec, exec, s[28:29]
	s_waitcnt vmcnt(0)
	s_and_saveexec_b64 s[28:29], s[8:9]
	s_cbranch_execz .Lcv_skipB_0
	v_lshlrev_b32_e32 v0, 16, v204
	v_and_b32_e32 v1, 0xffff0000, v204
	v_lshlrev_b32_e32 v2, 16, v205
	v_and_b32_e32 v3, 0xffff0000, v205
	v_lshlrev_b32_e32 v4, 16, v206
	v_and_b32_e32 v5, 0xffff0000, v206
	v_lshlrev_b32_e32 v6, 16, v207
	v_and_b32_e32 v7, 0xffff0000, v207
	ds_write_b128 v191, v[0:3]
	ds_write_b128 v191, v[4:7] offset:16
.Lcv_skipB_0:
	s_or_b64 exec, exec, s[28:29]
	s_and_saveexec_b64 s[28:29], s[10:11]
	s_cbranch_execz .Lcv_skipB_1
	v_lshlrev_b32_e32 v0, 16, v208
	v_and_b32_e32 v1, 0xffff0000, v208
	v_lshlrev_b32_e32 v2, 16, v209
	v_and_b32_e32 v3, 0xffff0000, v209
	v_lshlrev_b32_e32 v4, 16, v210
	v_and_b32_e32 v5, 0xffff0000, v210
	v_lshlrev_b32_e32 v6, 16, v211
	v_and_b32_e32 v7, 0xffff0000, v211
	ds_write_b128 v192, v[0:3]
	ds_write_b128 v192, v[4:7] offset:16
.Lcv_skipB_1:
	s_or_b64 exec, exec, s[28:29]
	s_and_saveexec_b64 s[28:29], s[12:13]
	s_cbranch_execz .Lcv_skipB_2
	v_lshlrev_b32_e32 v0, 16, v212
	v_and_b32_e32 v1, 0xffff0000, v212
	v_lshlrev_b32_e32 v2, 16, v213
	v_and_b32_e32 v3, 0xffff0000, v213
	v_lshlrev_b32_e32 v4, 16, v214
	v_and_b32_e32 v5, 0xffff0000, v214
	v_lshlrev_b32_e32 v6, 16, v215
	v_and_b32_e32 v7, 0xffff0000, v215
	ds_write_b128 v193, v[0:3]
	ds_write_b128 v193, v[4:7] offset:16
.Lcv_skipB_2:
	s_or_b64 exec, exec, s[28:29]
	s_and_saveexec_b64 s[28:29], s[14:15]
	s_cbranch_execz .Lcv_skipB_3
	v_lshlrev_b32_e32 v0, 16, v216
	v_and_b32_e32 v1, 0xffff0000, v216
	v_lshlrev_b32_e32 v2, 16, v217
	v_and_b32_e32 v3, 0xffff0000, v217
	v_lshlrev_b32_e32 v4, 16, v218
	v_and_b32_e32 v5, 0xffff0000, v218
	v_lshlrev_b32_e32 v6, 16, v219
	v_and_b32_e32 v7, 0xffff0000, v219
	ds_write_b128 v194, v[0:3]
	ds_write_b128 v194, v[4:7] offset:16
.Lcv_skipB_3:
	s_or_b64 exec, exec, s[28:29]
	s_and_saveexec_b64 s[28:29], s[16:17]
	s_cbranch_execz .Lcv_skipB_4
	v_lshlrev_b32_e32 v0, 16, v220
	v_and_b32_e32 v1, 0xffff0000, v220
	v_lshlrev_b32_e32 v2, 16, v221
	v_and_b32_e32 v3, 0xffff0000, v221
	v_lshlrev_b32_e32 v4, 16, v222
	v_and_b32_e32 v5, 0xffff0000, v222
	v_lshlrev_b32_e32 v6, 16, v223
	v_and_b32_e32 v7, 0xffff0000, v223
	ds_write_b128 v195, v[0:3]
	ds_write_b128 v195, v[4:7] offset:16
.Lcv_skipB_4:
	s_or_b64 exec, exec, s[28:29]
	s_and_saveexec_b64 s[28:29], s[18:19]
	s_cbranch_execz .Lcv_skipB_5
	v_lshlrev_b32_e32 v0, 16, v224
	v_and_b32_e32 v1, 0xffff0000, v224
	v_lshlrev_b32_e32 v2, 16, v225
	v_and_b32_e32 v3, 0xffff0000, v225
	v_lshlrev_b32_e32 v4, 16, v226
	v_and_b32_e32 v5, 0xffff0000, v226
	v_lshlrev_b32_e32 v6, 16, v227
	v_and_b32_e32 v7, 0xffff0000, v227
	ds_write_b128 v196, v[0:3]
	ds_write_b128 v196, v[4:7] offset:16
.Lcv_skipB_5:
	s_or_b64 exec, exec, s[28:29]
	s_and_saveexec_b64 s[28:29], s[20:21]
	s_cbranch_execz .Lcv_skipB_6
	v_lshlrev_b32_e32 v0, 16, v230
	v_and_b32_e32 v1, 0xffff0000, v230
	v_lshlrev_b32_e32 v2, 16, v231
	v_and_b32_e32 v3, 0xffff0000, v231
	v_lshlrev_b32_e32 v4, 16, v232
	v_and_b32_e32 v5, 0xffff0000, v232
	v_lshlrev_b32_e32 v6, 16, v233
	v_and_b32_e32 v7, 0xffff0000, v233
	ds_write_b128 v197, v[0:3]
	ds_write_b128 v197, v[4:7] offset:16
.Lcv_skipB_6:
	s_or_b64 exec, exec, s[28:29]
	s_and_saveexec_b64 s[28:29], s[22:23]
	s_cbranch_execz .Lcv_skipB_7
	v_lshlrev_b32_e32 v0, 16, v234
	v_and_b32_e32 v1, 0xffff0000, v234
	v_lshlrev_b32_e32 v2, 16, v235
	v_and_b32_e32 v3, 0xffff0000, v235
	v_lshlrev_b32_e32 v4, 16, v236
	v_and_b32_e32 v5, 0xffff0000, v236
	v_lshlrev_b32_e32 v6, 16, v237
	v_and_b32_e32 v7, 0xffff0000, v237
	ds_write_b128 v198, v[0:3]
	ds_write_b128 v198, v[4:7] offset:16
